# branch-gate GEMM sigmoid epilogue regenerated stage-major with packed f32 fma (in place on accumulators), second-half bias loads hoisted; same math
# speedup vs baseline: 1.0103x; 1.0050x over previous
.LBB0_669:
	v_mov_b32_e32 v0, v215
	s_nop 15
	s_nop 15
	s_mul_i32 s30, s36, 0x2200000
	v_readfirstlane_b32 s71, v0
	s_bfe_u32 s28, s71, 0x20006
	s_mul_hi_i32 s29, s36, 0x2200000
	s_add_u32 s82, s16, s30
	v_and_b32_e32 v11, 15, v0
	v_bfe_u32 v0, v0, 4, 2
	s_addc_u32 s83, s17, s29
	s_lshl_b32 s73, s28, 5
	v_lshlrev_b32_e32 v10, 3, v0
	s_cmp_gt_i32 s36, 11
	s_mov_b64 s[50:51], -1
	s_mov_b32 s37, s8
	s_cbranch_scc0 .LBB0_671
	s_ashr_i32 s75, s74, 31
	s_lshl_b64 s[30:31], s[74:75], 16
	s_add_u32 s30, s82, s30
	s_addc_u32 s31, s83, s31
	s_and_b32 s29, s71, 0xfffff00
	s_lshl_b32 s28, s28, 6
	s_or_b32 s28, s28, s29
	v_lshlrev_b32_e32 v0, 4, v0
	v_or3_b32 v0, s28, v0, v11
	s_lshl_b32 s28, s36, 8
	s_add_i32 s28, s28, 0x7ffff400
	s_and_b32 s28, s28, 0x7ffffc00
	s_mov_b32 s29, s5
	v_lshlrev_b32_e32 v0, 4, v0
	s_lshl_b64 s[28:29], s[28:29], 2
	v_ashrrev_i32_e32 v1, 31, v0
	s_add_u32 s28, s15, s28
	v_lshl_add_u64 v[8:9], s[30:31], 0, v[0:1]
	s_addc_u32 s29, s25, s29
	s_lshl_b32 s30, s36, 10
	s_and_b32 s30, s30, 0xc00
	s_add_u32 s28, s28, s30
	s_addc_u32 s29, s29, 0
	s_lshl_b32 s30, s73, 2
	s_add_u32 s96, s28, s30
	s_addc_u32 s97, s29, 0
	v_lshlrev_b32_e32 v12, 2, v10
	global_load_dwordx4 v[0:3], v12, s[96:97] offset:16
	global_load_dwordx4 v[4:7], v12, s[96:97]
	s_mov_b32 s28, 0xa000
	s_mov_b64 s[50:51], 0
	s_waitcnt vmcnt(0)
	s_mov_b32 s98, 0xbfb8aa3b
	s_mov_b32 s99, 0x3b808081
	global_load_dwordx4 v[240:243], v12, s[96:97] offset:528
	global_load_dwordx4 v[244:247], v12, s[96:97] offset:512
	v_pk_mul_f32 v[0:1], v[0:1], s[98:99] op_sel_hi:[1,0]
	v_pk_mul_f32 v[2:3], v[2:3], s[98:99] op_sel_hi:[1,0]
	v_pk_mul_f32 v[4:5], v[4:5], s[98:99] op_sel_hi:[1,0]
	v_pk_mul_f32 v[6:7], v[6:7], s[98:99] op_sel_hi:[1,0]
	v_pk_fma_f32 v[158:159], v[158:159], s[98:99], v[4:5] op_sel_hi:[1,0,1]
	v_pk_fma_f32 v[160:161], v[160:161], s[98:99], v[6:7] op_sel_hi:[1,0,1]
	v_pk_fma_f32 v[154:155], v[154:155], s[98:99], v[0:1] op_sel_hi:[1,0,1]
	v_pk_fma_f32 v[156:157], v[156:157], s[98:99], v[2:3] op_sel_hi:[1,0,1]
	v_pk_fma_f32 v[150:151], v[150:151], s[98:99], v[4:5] op_sel_hi:[1,0,1]
	v_pk_fma_f32 v[152:153], v[152:153], s[98:99], v[6:7] op_sel_hi:[1,0,1]
	v_pk_fma_f32 v[146:147], v[146:147], s[98:99], v[0:1] op_sel_hi:[1,0,1]
	v_pk_fma_f32 v[148:149], v[148:149], s[98:99], v[2:3] op_sel_hi:[1,0,1]
	v_exp_f32_e32 v158, v158
	v_exp_f32_e32 v159, v159
	v_exp_f32_e32 v160, v160
	v_exp_f32_e32 v161, v161
	v_exp_f32_e32 v154, v154
	v_exp_f32_e32 v155, v155
	v_exp_f32_e32 v156, v156
	v_exp_f32_e32 v157, v157
	v_exp_f32_e32 v150, v150
	v_exp_f32_e32 v151, v151
	v_exp_f32_e32 v152, v152
	v_exp_f32_e32 v153, v153
	v_exp_f32_e32 v146, v146
	v_exp_f32_e32 v147, v147
	v_exp_f32_e32 v148, v148
	v_exp_f32_e32 v149, v149
	v_pk_fma_f32 v[158:159], v[158:159], s[98:99], v[198:199] op_sel:[0,1,0] op_sel_hi:[1,1,0]
	v_pk_fma_f32 v[160:161], v[160:161], s[98:99], v[198:199] op_sel:[0,1,0] op_sel_hi:[1,1,0]
	v_pk_fma_f32 v[154:155], v[154:155], s[98:99], v[198:199] op_sel:[0,1,0] op_sel_hi:[1,1,0]
	v_pk_fma_f32 v[156:157], v[156:157], s[98:99], v[198:199] op_sel:[0,1,0] op_sel_hi:[1,1,0]
	v_pk_fma_f32 v[150:151], v[150:151], s[98:99], v[198:199] op_sel:[0,1,0] op_sel_hi:[1,1,0]
	v_pk_fma_f32 v[152:153], v[152:153], s[98:99], v[198:199] op_sel:[0,1,0] op_sel_hi:[1,1,0]
	v_pk_fma_f32 v[146:147], v[146:147], s[98:99], v[198:199] op_sel:[0,1,0] op_sel_hi:[1,1,0]
	v_pk_fma_f32 v[148:149], v[148:149], s[98:99], v[198:199] op_sel:[0,1,0] op_sel_hi:[1,1,0]
	v_rcp_f32_e32 v158, v158
	v_rcp_f32_e32 v159, v159
	v_rcp_f32_e32 v160, v160
	v_rcp_f32_e32 v161, v161
	v_rcp_f32_e32 v154, v154
	v_rcp_f32_e32 v155, v155
	v_rcp_f32_e32 v156, v156
	v_rcp_f32_e32 v157, v157
	v_rcp_f32_e32 v150, v150
	v_rcp_f32_e32 v151, v151
	v_rcp_f32_e32 v152, v152
	v_rcp_f32_e32 v153, v153
	v_rcp_f32_e32 v146, v146
	v_rcp_f32_e32 v147, v147
	v_rcp_f32_e32 v148, v148
	v_rcp_f32_e32 v149, v149
	v_cvt_pk_u8_f32 v14, v158, 0, 0
	v_cvt_pk_u8_f32 v14, v159, 1, v14
	v_cvt_pk_u8_f32 v14, v160, 2, v14
	v_cvt_pk_u8_f32 v14, v161, 3, v14
	v_cvt_pk_u8_f32 v15, v154, 0, 0
	v_cvt_pk_u8_f32 v15, v155, 1, v15
	v_cvt_pk_u8_f32 v15, v156, 2, v15
	v_cvt_pk_u8_f32 v15, v157, 3, v15
	v_cvt_pk_u8_f32 v16, v150, 0, 0
	v_cvt_pk_u8_f32 v16, v151, 1, v16
	v_cvt_pk_u8_f32 v16, v152, 2, v16
	v_cvt_pk_u8_f32 v16, v153, 3, v16
	v_cvt_pk_u8_f32 v17, v146, 0, 0
	v_cvt_pk_u8_f32 v17, v147, 1, v17
	v_cvt_pk_u8_f32 v17, v148, 2, v17
	v_cvt_pk_u8_f32 v17, v149, 3, v17
	v_or_b32_e32 v14, 0x1010101, v14
	v_or_b32_e32 v15, 0x1010101, v15
	v_or_b32_e32 v16, 0x1010101, v16
	v_or_b32_e32 v17, 0x1010101, v17
	global_store_dwordx4 v[8:9], v[14:17], off
	v_add_co_u32_e32 v18, vcc, s59, v8
	v_addc_co_u32_e32 v19, vcc, 0, v9, vcc
	v_pk_fma_f32 v[134:135], v[134:135], s[98:99], v[4:5] op_sel_hi:[1,0,1]
	v_pk_fma_f32 v[136:137], v[136:137], s[98:99], v[6:7] op_sel_hi:[1,0,1]
	v_pk_fma_f32 v[130:131], v[130:131], s[98:99], v[0:1] op_sel_hi:[1,0,1]
	v_pk_fma_f32 v[132:133], v[132:133], s[98:99], v[2:3] op_sel_hi:[1,0,1]
	v_pk_fma_f32 v[118:119], v[118:119], s[98:99], v[4:5] op_sel_hi:[1,0,1]
	v_pk_fma_f32 v[120:121], v[120:121], s[98:99], v[6:7] op_sel_hi:[1,0,1]
	v_pk_fma_f32 v[114:115], v[114:115], s[98:99], v[0:1] op_sel_hi:[1,0,1]
	v_pk_fma_f32 v[116:117], v[116:117], s[98:99], v[2:3] op_sel_hi:[1,0,1]
	v_exp_f32_e32 v134, v134
	v_exp_f32_e32 v135, v135
	v_exp_f32_e32 v136, v136
	v_exp_f32_e32 v137, v137
	v_exp_f32_e32 v130, v130
	v_exp_f32_e32 v131, v131
	v_exp_f32_e32 v132, v132
	v_exp_f32_e32 v133, v133
	v_exp_f32_e32 v118, v118
	v_exp_f32_e32 v119, v119
	v_exp_f32_e32 v120, v120
	v_exp_f32_e32 v121, v121
	v_exp_f32_e32 v114, v114
	v_exp_f32_e32 v115, v115
	v_exp_f32_e32 v116, v116
	v_exp_f32_e32 v117, v117
	v_pk_fma_f32 v[134:135], v[134:135], s[98:99], v[198:199] op_sel:[0,1,0] op_sel_hi:[1,1,0]
	v_pk_fma_f32 v[136:137], v[136:137], s[98:99], v[198:199] op_sel:[0,1,0] op_sel_hi:[1,1,0]
	v_pk_fma_f32 v[130:131], v[130:131], s[98:99], v[198:199] op_sel:[0,1,0] op_sel_hi:[1,1,0]
	v_pk_fma_f32 v[132:133], v[132:133], s[98:99], v[198:199] op_sel:[0,1,0] op_sel_hi:[1,1,0]
	v_pk_fma_f32 v[118:119], v[118:119], s[98:99], v[198:199] op_sel:[0,1,0] op_sel_hi:[1,1,0]
	v_pk_fma_f32 v[120:121], v[120:121], s[98:99], v[198:199] op_sel:[0,1,0] op_sel_hi:[1,1,0]
	v_pk_fma_f32 v[114:115], v[114:115], s[98:99], v[198:199] op_sel:[0,1,0] op_sel_hi:[1,1,0]
	v_pk_fma_f32 v[116:117], v[116:117], s[98:99], v[198:199] op_sel:[0,1,0] op_sel_hi:[1,1,0]
	v_rcp_f32_e32 v134, v134
	v_rcp_f32_e32 v135, v135
	v_rcp_f32_e32 v136, v136
	v_rcp_f32_e32 v137, v137
	v_rcp_f32_e32 v130, v130
	v_rcp_f32_e32 v131, v131
	v_rcp_f32_e32 v132, v132
	v_rcp_f32_e32 v133, v133
	v_rcp_f32_e32 v118, v118
	v_rcp_f32_e32 v119, v119
	v_rcp_f32_e32 v120, v120
	v_rcp_f32_e32 v121, v121
	v_rcp_f32_e32 v114, v114
	v_rcp_f32_e32 v115, v115
	v_rcp_f32_e32 v116, v116
	v_rcp_f32_e32 v117, v117
	v_cvt_pk_u8_f32 v14, v134, 0, 0
	v_cvt_pk_u8_f32 v14, v135, 1, v14
	v_cvt_pk_u8_f32 v14, v136, 2, v14
	v_cvt_pk_u8_f32 v14, v137, 3, v14
	v_cvt_pk_u8_f32 v15, v130, 0, 0
	v_cvt_pk_u8_f32 v15, v131, 1, v15
	v_cvt_pk_u8_f32 v15, v132, 2, v15
	v_cvt_pk_u8_f32 v15, v133, 3, v15
	v_cvt_pk_u8_f32 v16, v118, 0, 0
	v_cvt_pk_u8_f32 v16, v119, 1, v16
	v_cvt_pk_u8_f32 v16, v120, 2, v16
	v_cvt_pk_u8_f32 v16, v121, 3, v16
	v_cvt_pk_u8_f32 v17, v114, 0, 0
	v_cvt_pk_u8_f32 v17, v115, 1, v17
	v_cvt_pk_u8_f32 v17, v116, 2, v17
	v_cvt_pk_u8_f32 v17, v117, 3, v17
	v_or_b32_e32 v14, 0x1010101, v14
	v_or_b32_e32 v15, 0x1010101, v15
	v_or_b32_e32 v16, 0x1010101, v16
	v_or_b32_e32 v17, 0x1010101, v17
	global_store_dwordx4 v[18:19], v[14:17], off
	v_add_co_u32_e32 v18, vcc, s62, v8
	v_addc_co_u32_e32 v19, vcc, 0, v9, vcc
	v_pk_fma_f32 v[92:93], v[92:93], s[98:99], v[4:5] op_sel_hi:[1,0,1]
	v_pk_fma_f32 v[94:95], v[94:95], s[98:99], v[6:7] op_sel_hi:[1,0,1]
	v_pk_fma_f32 v[88:89], v[88:89], s[98:99], v[0:1] op_sel_hi:[1,0,1]
	v_pk_fma_f32 v[90:91], v[90:91], s[98:99], v[2:3] op_sel_hi:[1,0,1]
	v_pk_fma_f32 v[84:85], v[84:85], s[98:99], v[4:5] op_sel_hi:[1,0,1]
	v_pk_fma_f32 v[86:87], v[86:87], s[98:99], v[6:7] op_sel_hi:[1,0,1]
	v_pk_fma_f32 v[80:81], v[80:81], s[98:99], v[0:1] op_sel_hi:[1,0,1]
	v_pk_fma_f32 v[82:83], v[82:83], s[98:99], v[2:3] op_sel_hi:[1,0,1]
	v_exp_f32_e32 v92, v92
	v_exp_f32_e32 v93, v93
	v_exp_f32_e32 v94, v94
	v_exp_f32_e32 v95, v95
	v_exp_f32_e32 v88, v88
	v_exp_f32_e32 v89, v89
	v_exp_f32_e32 v90, v90
	v_exp_f32_e32 v91, v91
	v_exp_f32_e32 v84, v84
	v_exp_f32_e32 v85, v85
	v_exp_f32_e32 v86, v86
	v_exp_f32_e32 v87, v87
	v_exp_f32_e32 v80, v80
	v_exp_f32_e32 v81, v81
	v_exp_f32_e32 v82, v82
	v_exp_f32_e32 v83, v83
	v_pk_fma_f32 v[92:93], v[92:93], s[98:99], v[198:199] op_sel:[0,1,0] op_sel_hi:[1,1,0]
	v_pk_fma_f32 v[94:95], v[94:95], s[98:99], v[198:199] op_sel:[0,1,0] op_sel_hi:[1,1,0]
	v_pk_fma_f32 v[88:89], v[88:89], s[98:99], v[198:199] op_sel:[0,1,0] op_sel_hi:[1,1,0]
	v_pk_fma_f32 v[90:91], v[90:91], s[98:99], v[198:199] op_sel:[0,1,0] op_sel_hi:[1,1,0]
	v_pk_fma_f32 v[84:85], v[84:85], s[98:99], v[198:199] op_sel:[0,1,0] op_sel_hi:[1,1,0]
	v_pk_fma_f32 v[86:87], v[86:87], s[98:99], v[198:199] op_sel:[0,1,0] op_sel_hi:[1,1,0]
	v_pk_fma_f32 v[80:81], v[80:81], s[98:99], v[198:199] op_sel:[0,1,0] op_sel_hi:[1,1,0]
	v_pk_fma_f32 v[82:83], v[82:83], s[98:99], v[198:199] op_sel:[0,1,0] op_sel_hi:[1,1,0]
	v_rcp_f32_e32 v92, v92
	v_rcp_f32_e32 v93, v93
	v_rcp_f32_e32 v94, v94
	v_rcp_f32_e32 v95, v95
	v_rcp_f32_e32 v88, v88
	v_rcp_f32_e32 v89, v89
	v_rcp_f32_e32 v90, v90
	v_rcp_f32_e32 v91, v91
	v_rcp_f32_e32 v84, v84
	v_rcp_f32_e32 v85, v85
	v_rcp_f32_e32 v86, v86
	v_rcp_f32_e32 v87, v87
	v_rcp_f32_e32 v80, v80
	v_rcp_f32_e32 v81, v81
	v_rcp_f32_e32 v82, v82
	v_rcp_f32_e32 v83, v83
	v_cvt_pk_u8_f32 v14, v92, 0, 0
	v_cvt_pk_u8_f32 v14, v93, 1, v14
	v_cvt_pk_u8_f32 v14, v94, 2, v14
	v_cvt_pk_u8_f32 v14, v95, 3, v14
	v_cvt_pk_u8_f32 v15, v88, 0, 0
	v_cvt_pk_u8_f32 v15, v89, 1, v15
	v_cvt_pk_u8_f32 v15, v90, 2, v15
	v_cvt_pk_u8_f32 v15, v91, 3, v15
	v_cvt_pk_u8_f32 v16, v84, 0, 0
	v_cvt_pk_u8_f32 v16, v85, 1, v16
	v_cvt_pk_u8_f32 v16, v86, 2, v16
	v_cvt_pk_u8_f32 v16, v87, 3, v16
	v_cvt_pk_u8_f32 v17, v80, 0, 0
	v_cvt_pk_u8_f32 v17, v81, 1, v17
	v_cvt_pk_u8_f32 v17, v82, 2, v17
	v_cvt_pk_u8_f32 v17, v83, 3, v17
	v_or_b32_e32 v14, 0x1010101, v14
	v_or_b32_e32 v15, 0x1010101, v15
	v_or_b32_e32 v16, 0x1010101, v16
	v_or_b32_e32 v17, 0x1010101, v17
	global_store_dwordx4 v[18:19], v[14:17], off
	v_add_co_u32_e32 v18, vcc, s89, v8
	v_addc_co_u32_e32 v19, vcc, 0, v9, vcc
	v_pk_fma_f32 v[68:69], v[68:69], s[98:99], v[4:5] op_sel_hi:[1,0,1]
	v_pk_fma_f32 v[70:71], v[70:71], s[98:99], v[6:7] op_sel_hi:[1,0,1]
	v_pk_fma_f32 v[64:65], v[64:65], s[98:99], v[0:1] op_sel_hi:[1,0,1]
	v_pk_fma_f32 v[66:67], v[66:67], s[98:99], v[2:3] op_sel_hi:[1,0,1]
	v_pk_fma_f32 v[52:53], v[52:53], s[98:99], v[4:5] op_sel_hi:[1,0,1]
	v_pk_fma_f32 v[54:55], v[54:55], s[98:99], v[6:7] op_sel_hi:[1,0,1]
	v_pk_fma_f32 v[48:49], v[48:49], s[98:99], v[0:1] op_sel_hi:[1,0,1]
	v_pk_fma_f32 v[50:51], v[50:51], s[98:99], v[2:3] op_sel_hi:[1,0,1]
	v_exp_f32_e32 v68, v68
	v_exp_f32_e32 v69, v69
	v_exp_f32_e32 v70, v70
	v_exp_f32_e32 v71, v71
	v_exp_f32_e32 v64, v64
	v_exp_f32_e32 v65, v65
	v_exp_f32_e32 v66, v66
	v_exp_f32_e32 v67, v67
	v_exp_f32_e32 v52, v52
	v_exp_f32_e32 v53, v53
	v_exp_f32_e32 v54, v54
	v_exp_f32_e32 v55, v55
	v_exp_f32_e32 v48, v48
	v_exp_f32_e32 v49, v49
	v_exp_f32_e32 v50, v50
	v_exp_f32_e32 v51, v51
	v_pk_fma_f32 v[68:69], v[68:69], s[98:99], v[198:199] op_sel:[0,1,0] op_sel_hi:[1,1,0]
	v_pk_fma_f32 v[70:71], v[70:71], s[98:99], v[198:199] op_sel:[0,1,0] op_sel_hi:[1,1,0]
	v_pk_fma_f32 v[64:65], v[64:65], s[98:99], v[198:199] op_sel:[0,1,0] op_sel_hi:[1,1,0]
	v_pk_fma_f32 v[66:67], v[66:67], s[98:99], v[198:199] op_sel:[0,1,0] op_sel_hi:[1,1,0]
	v_pk_fma_f32 v[52:53], v[52:53], s[98:99], v[198:199] op_sel:[0,1,0] op_sel_hi:[1,1,0]
	v_pk_fma_f32 v[54:55], v[54:55], s[98:99], v[198:199] op_sel:[0,1,0] op_sel_hi:[1,1,0]
	v_pk_fma_f32 v[48:49], v[48:49], s[98:99], v[198:199] op_sel:[0,1,0] op_sel_hi:[1,1,0]
	v_pk_fma_f32 v[50:51], v[50:51], s[98:99], v[198:199] op_sel:[0,1,0] op_sel_hi:[1,1,0]
	v_rcp_f32_e32 v68, v68
	v_rcp_f32_e32 v69, v69
	v_rcp_f32_e32 v70, v70
	v_rcp_f32_e32 v71, v71
	v_rcp_f32_e32 v64, v64
	v_rcp_f32_e32 v65, v65
	v_rcp_f32_e32 v66, v66
	v_rcp_f32_e32 v67, v67
	v_rcp_f32_e32 v52, v52
	v_rcp_f32_e32 v53, v53
	v_rcp_f32_e32 v54, v54
	v_rcp_f32_e32 v55, v55
	v_rcp_f32_e32 v48, v48
	v_rcp_f32_e32 v49, v49
	v_rcp_f32_e32 v50, v50
	v_rcp_f32_e32 v51, v51
	v_cvt_pk_u8_f32 v14, v68, 0, 0
	v_cvt_pk_u8_f32 v14, v69, 1, v14
	v_cvt_pk_u8_f32 v14, v70, 2, v14
	v_cvt_pk_u8_f32 v14, v71, 3, v14
	v_cvt_pk_u8_f32 v15, v64, 0, 0
	v_cvt_pk_u8_f32 v15, v65, 1, v15
	v_cvt_pk_u8_f32 v15, v66, 2, v15
	v_cvt_pk_u8_f32 v15, v67, 3, v15
	v_cvt_pk_u8_f32 v16, v52, 0, 0
	v_cvt_pk_u8_f32 v16, v53, 1, v16
	v_cvt_pk_u8_f32 v16, v54, 2, v16
	v_cvt_pk_u8_f32 v16, v55, 3, v16
	v_cvt_pk_u8_f32 v17, v48, 0, 0
	v_cvt_pk_u8_f32 v17, v49, 1, v17
	v_cvt_pk_u8_f32 v17, v50, 2, v17
	v_cvt_pk_u8_f32 v17, v51, 3, v17
	v_or_b32_e32 v14, 0x1010101, v14
	v_or_b32_e32 v15, 0x1010101, v15
	v_or_b32_e32 v16, 0x1010101, v16
	v_or_b32_e32 v17, 0x1010101, v17
	global_store_dwordx4 v[18:19], v[14:17], off
	v_add_co_u32_e32 v18, vcc, s24, v8
	v_addc_co_u32_e32 v19, vcc, 0, v9, vcc
	s_waitcnt vmcnt(4)
	v_pk_mul_f32 v[240:241], v[240:241], s[98:99] op_sel_hi:[1,0]
	v_pk_mul_f32 v[242:243], v[242:243], s[98:99] op_sel_hi:[1,0]
	v_pk_mul_f32 v[244:245], v[244:245], s[98:99] op_sel_hi:[1,0]
	v_pk_mul_f32 v[246:247], v[246:247], s[98:99] op_sel_hi:[1,0]
	v_pk_fma_f32 v[142:143], v[142:143], s[98:99], v[244:245] op_sel_hi:[1,0,1]
	v_pk_fma_f32 v[144:145], v[144:145], s[98:99], v[246:247] op_sel_hi:[1,0,1]
	v_pk_fma_f32 v[138:139], v[138:139], s[98:99], v[240:241] op_sel_hi:[1,0,1]
	v_pk_fma_f32 v[140:141], v[140:141], s[98:99], v[242:243] op_sel_hi:[1,0,1]
	v_pk_fma_f32 v[126:127], v[126:127], s[98:99], v[244:245] op_sel_hi:[1,0,1]
	v_pk_fma_f32 v[128:129], v[128:129], s[98:99], v[246:247] op_sel_hi:[1,0,1]
	v_pk_fma_f32 v[122:123], v[122:123], s[98:99], v[240:241] op_sel_hi:[1,0,1]
	v_pk_fma_f32 v[124:125], v[124:125], s[98:99], v[242:243] op_sel_hi:[1,0,1]
	v_exp_f32_e32 v142, v142
	v_exp_f32_e32 v143, v143
	v_exp_f32_e32 v144, v144
	v_exp_f32_e32 v145, v145
	v_exp_f32_e32 v138, v138
	v_exp_f32_e32 v139, v139
	v_exp_f32_e32 v140, v140
	v_exp_f32_e32 v141, v141
	v_exp_f32_e32 v126, v126
	v_exp_f32_e32 v127, v127
	v_exp_f32_e32 v128, v128
	v_exp_f32_e32 v129, v129
	v_exp_f32_e32 v122, v122
	v_exp_f32_e32 v123, v123
	v_exp_f32_e32 v124, v124
	v_exp_f32_e32 v125, v125
	v_pk_fma_f32 v[142:143], v[142:143], s[98:99], v[198:199] op_sel:[0,1,0] op_sel_hi:[1,1,0]
	v_pk_fma_f32 v[144:145], v[144:145], s[98:99], v[198:199] op_sel:[0,1,0] op_sel_hi:[1,1,0]
	v_pk_fma_f32 v[138:139], v[138:139], s[98:99], v[198:199] op_sel:[0,1,0] op_sel_hi:[1,1,0]
	v_pk_fma_f32 v[140:141], v[140:141], s[98:99], v[198:199] op_sel:[0,1,0] op_sel_hi:[1,1,0]
	v_pk_fma_f32 v[126:127], v[126:127], s[98:99], v[198:199] op_sel:[0,1,0] op_sel_hi:[1,1,0]
	v_pk_fma_f32 v[128:129], v[128:129], s[98:99], v[198:199] op_sel:[0,1,0] op_sel_hi:[1,1,0]
	v_pk_fma_f32 v[122:123], v[122:123], s[98:99], v[198:199] op_sel:[0,1,0] op_sel_hi:[1,1,0]
	v_pk_fma_f32 v[124:125], v[124:125], s[98:99], v[198:199] op_sel:[0,1,0] op_sel_hi:[1,1,0]
	v_rcp_f32_e32 v142, v142
	v_rcp_f32_e32 v143, v143
	v_rcp_f32_e32 v144, v144
	v_rcp_f32_e32 v145, v145
	v_rcp_f32_e32 v138, v138
	v_rcp_f32_e32 v139, v139
	v_rcp_f32_e32 v140, v140
	v_rcp_f32_e32 v141, v141
	v_rcp_f32_e32 v126, v126
	v_rcp_f32_e32 v127, v127
	v_rcp_f32_e32 v128, v128
	v_rcp_f32_e32 v129, v129
	v_rcp_f32_e32 v122, v122
	v_rcp_f32_e32 v123, v123
	v_rcp_f32_e32 v124, v124
	v_rcp_f32_e32 v125, v125
	v_cvt_pk_u8_f32 v14, v142, 0, 0
	v_cvt_pk_u8_f32 v14, v143, 1, v14
	v_cvt_pk_u8_f32 v14, v144, 2, v14
	v_cvt_pk_u8_f32 v14, v145, 3, v14
	v_cvt_pk_u8_f32 v15, v138, 0, 0
	v_cvt_pk_u8_f32 v15, v139, 1, v15
	v_cvt_pk_u8_f32 v15, v140, 2, v15
	v_cvt_pk_u8_f32 v15, v141, 3, v15
	v_cvt_pk_u8_f32 v16, v126, 0, 0
	v_cvt_pk_u8_f32 v16, v127, 1, v16
	v_cvt_pk_u8_f32 v16, v128, 2, v16
	v_cvt_pk_u8_f32 v16, v129, 3, v16
	v_cvt_pk_u8_f32 v17, v122, 0, 0
	v_cvt_pk_u8_f32 v17, v123, 1, v17
	v_cvt_pk_u8_f32 v17, v124, 2, v17
	v_cvt_pk_u8_f32 v17, v125, 3, v17
	v_or_b32_e32 v14, 0x1010101, v14
	v_or_b32_e32 v15, 0x1010101, v15
	v_or_b32_e32 v16, 0x1010101, v16
	v_or_b32_e32 v17, 0x1010101, v17
	global_store_dwordx4 v[18:19], v[14:17], off
	v_add_co_u32_e32 v18, vcc, s28, v8
	v_addc_co_u32_e32 v19, vcc, 0, v9, vcc
	v_pk_fma_f32 v[108:109], v[108:109], s[98:99], v[244:245] op_sel_hi:[1,0,1]
	v_pk_fma_f32 v[110:111], v[110:111], s[98:99], v[246:247] op_sel_hi:[1,0,1]
	v_pk_fma_f32 v[104:105], v[104:105], s[98:99], v[240:241] op_sel_hi:[1,0,1]
	v_pk_fma_f32 v[106:107], v[106:107], s[98:99], v[242:243] op_sel_hi:[1,0,1]
	v_pk_fma_f32 v[100:101], v[100:101], s[98:99], v[244:245] op_sel_hi:[1,0,1]
	v_pk_fma_f32 v[102:103], v[102:103], s[98:99], v[246:247] op_sel_hi:[1,0,1]
	v_pk_fma_f32 v[96:97], v[96:97], s[98:99], v[240:241] op_sel_hi:[1,0,1]
	v_pk_fma_f32 v[98:99], v[98:99], s[98:99], v[242:243] op_sel_hi:[1,0,1]
	v_exp_f32_e32 v108, v108
	v_exp_f32_e32 v109, v109
	v_exp_f32_e32 v110, v110
	v_exp_f32_e32 v111, v111
	v_exp_f32_e32 v104, v104
	v_exp_f32_e32 v105, v105
	v_exp_f32_e32 v106, v106
	v_exp_f32_e32 v107, v107
	v_exp_f32_e32 v100, v100
	v_exp_f32_e32 v101, v101
	v_exp_f32_e32 v102, v102
	v_exp_f32_e32 v103, v103
	v_exp_f32_e32 v96, v96
	v_exp_f32_e32 v97, v97
	v_exp_f32_e32 v98, v98
	v_exp_f32_e32 v99, v99
	v_pk_fma_f32 v[108:109], v[108:109], s[98:99], v[198:199] op_sel:[0,1,0] op_sel_hi:[1,1,0]
	v_pk_fma_f32 v[110:111], v[110:111], s[98:99], v[198:199] op_sel:[0,1,0] op_sel_hi:[1,1,0]
	v_pk_fma_f32 v[104:105], v[104:105], s[98:99], v[198:199] op_sel:[0,1,0] op_sel_hi:[1,1,0]
	v_pk_fma_f32 v[106:107], v[106:107], s[98:99], v[198:199] op_sel:[0,1,0] op_sel_hi:[1,1,0]
	v_pk_fma_f32 v[100:101], v[100:101], s[98:99], v[198:199] op_sel:[0,1,0] op_sel_hi:[1,1,0]
	v_pk_fma_f32 v[102:103], v[102:103], s[98:99], v[198:199] op_sel:[0,1,0] op_sel_hi:[1,1,0]
	v_pk_fma_f32 v[96:97], v[96:97], s[98:99], v[198:199] op_sel:[0,1,0] op_sel_hi:[1,1,0]
	v_pk_fma_f32 v[98:99], v[98:99], s[98:99], v[198:199] op_sel:[0,1,0] op_sel_hi:[1,1,0]
	v_rcp_f32_e32 v108, v108
	v_rcp_f32_e32 v109, v109
	v_rcp_f32_e32 v110, v110
	v_rcp_f32_e32 v111, v111
	v_rcp_f32_e32 v104, v104
	v_rcp_f32_e32 v105, v105
	v_rcp_f32_e32 v106, v106
	v_rcp_f32_e32 v107, v107
	v_rcp_f32_e32 v100, v100
	v_rcp_f32_e32 v101, v101
	v_rcp_f32_e32 v102, v102
	v_rcp_f32_e32 v103, v103
	v_rcp_f32_e32 v96, v96
	v_rcp_f32_e32 v97, v97
	v_rcp_f32_e32 v98, v98
	v_rcp_f32_e32 v99, v99
	v_cvt_pk_u8_f32 v14, v108, 0, 0
	v_cvt_pk_u8_f32 v14, v109, 1, v14
	v_cvt_pk_u8_f32 v14, v110, 2, v14
	v_cvt_pk_u8_f32 v14, v111, 3, v14
	v_cvt_pk_u8_f32 v15, v104, 0, 0
	v_cvt_pk_u8_f32 v15, v105, 1, v15
	v_cvt_pk_u8_f32 v15, v106, 2, v15
	v_cvt_pk_u8_f32 v15, v107, 3, v15
	v_cvt_pk_u8_f32 v16, v100, 0, 0
	v_cvt_pk_u8_f32 v16, v101, 1, v16
	v_cvt_pk_u8_f32 v16, v102, 2, v16
	v_cvt_pk_u8_f32 v16, v103, 3, v16
	v_cvt_pk_u8_f32 v17, v96, 0, 0
	v_cvt_pk_u8_f32 v17, v97, 1, v17
	v_cvt_pk_u8_f32 v17, v98, 2, v17
	v_cvt_pk_u8_f32 v17, v99, 3, v17
	v_or_b32_e32 v14, 0x1010101, v14
	v_or_b32_e32 v15, 0x1010101, v15
	v_or_b32_e32 v16, 0x1010101, v16
	v_or_b32_e32 v17, 0x1010101, v17
	global_store_dwordx4 v[18:19], v[14:17], off
	s_mov_b32 s28, 0xc000
	v_add_co_u32_e32 v18, vcc, s28, v8
	v_addc_co_u32_e32 v19, vcc, 0, v9, vcc
	v_pk_fma_f32 v[76:77], v[76:77], s[98:99], v[244:245] op_sel_hi:[1,0,1]
	v_pk_fma_f32 v[78:79], v[78:79], s[98:99], v[246:247] op_sel_hi:[1,0,1]
	v_pk_fma_f32 v[72:73], v[72:73], s[98:99], v[240:241] op_sel_hi:[1,0,1]
	v_pk_fma_f32 v[74:75], v[74:75], s[98:99], v[242:243] op_sel_hi:[1,0,1]
	v_pk_fma_f32 v[60:61], v[60:61], s[98:99], v[244:245] op_sel_hi:[1,0,1]
	v_pk_fma_f32 v[62:63], v[62:63], s[98:99], v[246:247] op_sel_hi:[1,0,1]
	v_pk_fma_f32 v[56:57], v[56:57], s[98:99], v[240:241] op_sel_hi:[1,0,1]
	v_pk_fma_f32 v[58:59], v[58:59], s[98:99], v[242:243] op_sel_hi:[1,0,1]
	v_exp_f32_e32 v76, v76
	v_exp_f32_e32 v77, v77
	v_exp_f32_e32 v78, v78
	v_exp_f32_e32 v79, v79
	v_exp_f32_e32 v72, v72
	v_exp_f32_e32 v73, v73
	v_exp_f32_e32 v74, v74
	v_exp_f32_e32 v75, v75
	v_exp_f32_e32 v60, v60
	v_exp_f32_e32 v61, v61
	v_exp_f32_e32 v62, v62
	v_exp_f32_e32 v63, v63
	v_exp_f32_e32 v56, v56
	v_exp_f32_e32 v57, v57
	v_exp_f32_e32 v58, v58
	v_exp_f32_e32 v59, v59
	v_pk_fma_f32 v[76:77], v[76:77], s[98:99], v[198:199] op_sel:[0,1,0] op_sel_hi:[1,1,0]
	v_pk_fma_f32 v[78:79], v[78:79], s[98:99], v[198:199] op_sel:[0,1,0] op_sel_hi:[1,1,0]
	v_pk_fma_f32 v[72:73], v[72:73], s[98:99], v[198:199] op_sel:[0,1,0] op_sel_hi:[1,1,0]
	v_pk_fma_f32 v[74:75], v[74:75], s[98:99], v[198:199] op_sel:[0,1,0] op_sel_hi:[1,1,0]
	v_pk_fma_f32 v[60:61], v[60:61], s[98:99], v[198:199] op_sel:[0,1,0] op_sel_hi:[1,1,0]
	v_pk_fma_f32 v[62:63], v[62:63], s[98:99], v[198:199] op_sel:[0,1,0] op_sel_hi:[1,1,0]
	v_pk_fma_f32 v[56:57], v[56:57], s[98:99], v[198:199] op_sel:[0,1,0] op_sel_hi:[1,1,0]
	v_pk_fma_f32 v[58:59], v[58:59], s[98:99], v[198:199] op_sel:[0,1,0] op_sel_hi:[1,1,0]
	v_rcp_f32_e32 v76, v76
	v_rcp_f32_e32 v77, v77
	v_rcp_f32_e32 v78, v78
	v_rcp_f32_e32 v79, v79
	v_rcp_f32_e32 v72, v72
	v_rcp_f32_e32 v73, v73
	v_rcp_f32_e32 v74, v74
	v_rcp_f32_e32 v75, v75
	v_rcp_f32_e32 v60, v60
	v_rcp_f32_e32 v61, v61
	v_rcp_f32_e32 v62, v62
	v_rcp_f32_e32 v63, v63
	v_rcp_f32_e32 v56, v56
	v_rcp_f32_e32 v57, v57
	v_rcp_f32_e32 v58, v58
	v_rcp_f32_e32 v59, v59
	v_cvt_pk_u8_f32 v14, v76, 0, 0
	v_cvt_pk_u8_f32 v14, v77, 1, v14
	v_cvt_pk_u8_f32 v14, v78, 2, v14
	v_cvt_pk_u8_f32 v14, v79, 3, v14
	v_cvt_pk_u8_f32 v15, v72, 0, 0
	v_cvt_pk_u8_f32 v15, v73, 1, v15
	v_cvt_pk_u8_f32 v15, v74, 2, v15
	v_cvt_pk_u8_f32 v15, v75, 3, v15
	v_cvt_pk_u8_f32 v16, v60, 0, 0
	v_cvt_pk_u8_f32 v16, v61, 1, v16
	v_cvt_pk_u8_f32 v16, v62, 2, v16
	v_cvt_pk_u8_f32 v16, v63, 3, v16
	v_cvt_pk_u8_f32 v17, v56, 0, 0
	v_cvt_pk_u8_f32 v17, v57, 1, v17
	v_cvt_pk_u8_f32 v17, v58, 2, v17
	v_cvt_pk_u8_f32 v17, v59, 3, v17
	v_or_b32_e32 v14, 0x1010101, v14
	v_or_b32_e32 v15, 0x1010101, v15
	v_or_b32_e32 v16, 0x1010101, v16
	v_or_b32_e32 v17, 0x1010101, v17
	global_store_dwordx4 v[18:19], v[14:17], off
	v_add_co_u32_e32 v18, vcc, 0xe000, v8
	v_addc_co_u32_e32 v19, vcc, 0, v9, vcc
	v_pk_fma_f32 v[44:45], v[44:45], s[98:99], v[244:245] op_sel_hi:[1,0,1]
	v_pk_fma_f32 v[46:47], v[46:47], s[98:99], v[246:247] op_sel_hi:[1,0,1]
	v_pk_fma_f32 v[40:41], v[40:41], s[98:99], v[240:241] op_sel_hi:[1,0,1]
	v_pk_fma_f32 v[42:43], v[42:43], s[98:99], v[242:243] op_sel_hi:[1,0,1]
	v_pk_fma_f32 v[36:37], v[36:37], s[98:99], v[244:245] op_sel_hi:[1,0,1]
	v_pk_fma_f32 v[38:39], v[38:39], s[98:99], v[246:247] op_sel_hi:[1,0,1]
	v_pk_fma_f32 v[32:33], v[32:33], s[98:99], v[240:241] op_sel_hi:[1,0,1]
	v_pk_fma_f32 v[34:35], v[34:35], s[98:99], v[242:243] op_sel_hi:[1,0,1]
	v_exp_f32_e32 v44, v44
	v_exp_f32_e32 v45, v45
	v_exp_f32_e32 v46, v46
	v_exp_f32_e32 v47, v47
	v_exp_f32_e32 v40, v40
	v_exp_f32_e32 v41, v41
	v_exp_f32_e32 v42, v42
	v_exp_f32_e32 v43, v43
	v_exp_f32_e32 v36, v36
	v_exp_f32_e32 v37, v37
	v_exp_f32_e32 v38, v38
	v_exp_f32_e32 v39, v39
	v_exp_f32_e32 v32, v32
	v_exp_f32_e32 v33, v33
	v_exp_f32_e32 v34, v34
	v_exp_f32_e32 v35, v35
	v_pk_fma_f32 v[44:45], v[44:45], s[98:99], v[198:199] op_sel:[0,1,0] op_sel_hi:[1,1,0]
	v_pk_fma_f32 v[46:47], v[46:47], s[98:99], v[198:199] op_sel:[0,1,0] op_sel_hi:[1,1,0]
	v_pk_fma_f32 v[40:41], v[40:41], s[98:99], v[198:199] op_sel:[0,1,0] op_sel_hi:[1,1,0]
	v_pk_fma_f32 v[42:43], v[42:43], s[98:99], v[198:199] op_sel:[0,1,0] op_sel_hi:[1,1,0]
	v_pk_fma_f32 v[36:37], v[36:37], s[98:99], v[198:199] op_sel:[0,1,0] op_sel_hi:[1,1,0]
	v_pk_fma_f32 v[38:39], v[38:39], s[98:99], v[198:199] op_sel:[0,1,0] op_sel_hi:[1,1,0]
	v_pk_fma_f32 v[32:33], v[32:33], s[98:99], v[198:199] op_sel:[0,1,0] op_sel_hi:[1,1,0]
	v_pk_fma_f32 v[34:35], v[34:35], s[98:99], v[198:199] op_sel:[0,1,0] op_sel_hi:[1,1,0]
	v_rcp_f32_e32 v44, v44
	v_rcp_f32_e32 v45, v45
	v_rcp_f32_e32 v46, v46
	v_rcp_f32_e32 v47, v47
	v_rcp_f32_e32 v40, v40
	v_rcp_f32_e32 v41, v41
	v_rcp_f32_e32 v42, v42
	v_rcp_f32_e32 v43, v43
	v_rcp_f32_e32 v36, v36
	v_rcp_f32_e32 v37, v37
	v_rcp_f32_e32 v38, v38
	v_rcp_f32_e32 v39, v39
	v_rcp_f32_e32 v32, v32
	v_rcp_f32_e32 v33, v33
	v_rcp_f32_e32 v34, v34
	v_rcp_f32_e32 v35, v35
	v_cvt_pk_u8_f32 v14, v44, 0, 0
	v_cvt_pk_u8_f32 v14, v45, 1, v14
	v_cvt_pk_u8_f32 v14, v46, 2, v14
	v_cvt_pk_u8_f32 v14, v47, 3, v14
	v_cvt_pk_u8_f32 v15, v40, 0, 0
	v_cvt_pk_u8_f32 v15, v41, 1, v15
	v_cvt_pk_u8_f32 v15, v42, 2, v15
	v_cvt_pk_u8_f32 v15, v43, 3, v15
	v_cvt_pk_u8_f32 v16, v36, 0, 0
	v_cvt_pk_u8_f32 v16, v37, 1, v16
	v_cvt_pk_u8_f32 v16, v38, 2, v16
	v_cvt_pk_u8_f32 v16, v39, 3, v16
	v_cvt_pk_u8_f32 v17, v32, 0, 0
	v_cvt_pk_u8_f32 v17, v33, 1, v17
	v_cvt_pk_u8_f32 v17, v34, 2, v17
	v_cvt_pk_u8_f32 v17, v35, 3, v17
	v_or_b32_e32 v14, 0x1010101, v14
	v_or_b32_e32 v15, 0x1010101, v15
	v_or_b32_e32 v16, 0x1010101, v16
	v_or_b32_e32 v17, 0x1010101, v17
	global_store_dwordx4 v[18:19], v[14:17], off
